# DIFF attention: QK K-fragment reads prefetched into 8 distinct dead VGPR quads with counted lgkmcnt waits (instead of read->wait(0)->MFMA on one buffer)
# speedup vs baseline: 1.0189x; 1.0027x over previous
.LBB0_833:
	s_add_i32 s30, s72, -1
	s_cmp_ge_u32 s30, s90
	s_cbranch_scc1 .LBB0_846
	s_cmp_lt_u32 s72, s90
	v_cmp_eq_f32_e64 s[30:31], s1, v173
	s_cselect_b64 s[52:53], -1, 0
	s_cmp_ge_u32 s72, s90
	v_cndmask_b32_e64 v185, v173, 0, s[30:31]
	s_cbranch_scc1 .LBB0_836
	s_mul_i32 s34, s71, 0x6000
	v_add_u32_e32 v147, s34, v169
	ds_read_b128 v[148:151], v147
	v_xor_b32_e32 v98, 0x80000000, v185
	v_mov_b32_e32 v99, v98
	v_mov_b32_e32 v100, v98
	v_mov_b32_e32 v101, v98
	v_mov_b32_e32 v102, v98
	v_mov_b32_e32 v103, v98
	v_mov_b32_e32 v104, v98
	v_mov_b32_e32 v105, v98
	v_mov_b32_e32 v106, v98
	v_mov_b32_e32 v107, v98
	v_mov_b32_e32 v108, v98
	v_mov_b32_e32 v109, v98
	v_mov_b32_e32 v110, v98
	v_mov_b32_e32 v111, v98
	v_mov_b32_e32 v112, v98
	v_mov_b32_e32 v113, v98
	ds_read_b128 v[152:155], v147 offset:4096
	v_add_u32_e32 v147, s34, v170
	ds_read_b128 v[156:159], v147
	ds_read_b128 v[188:191], v147 offset:4096
	v_add_u32_e32 v147, s34, v171
	ds_read_b128 v[192:195], v147
	ds_read_b128 v[196:199], v147 offset:4096
	v_add_u32_e32 v147, s34, v172
	ds_read_b128 v[208:211], v147
	ds_read_b128 v[212:215], v147 offset:4096
	s_waitcnt lgkmcnt(7)
	s_nop 0
	v_mfma_f32_32x32x16_f16 v[114:129], v[148:151], v[130:133], v[98:113]
	s_waitcnt lgkmcnt(6)
	v_mfma_f32_32x32x16_f16 v[98:113], v[152:155], v[130:133], v[98:113]
	s_waitcnt lgkmcnt(5)
	v_mfma_f32_32x32x16_f16 v[114:129], v[156:159], v[134:137], v[114:129]
	s_waitcnt lgkmcnt(4)
	v_mfma_f32_32x32x16_f16 v[98:113], v[188:191], v[134:137], v[98:113]
	s_waitcnt lgkmcnt(3)
	v_mfma_f32_32x32x16_f16 v[114:129], v[192:195], v[138:141], v[114:129]
	s_waitcnt lgkmcnt(2)
	v_mfma_f32_32x32x16_f16 v[98:113], v[196:199], v[138:141], v[98:113]
	s_waitcnt lgkmcnt(1)
	v_mfma_f32_32x32x16_f16 v[114:129], v[208:211], v[142:145], v[114:129]
	s_waitcnt lgkmcnt(0)
	v_mfma_f32_32x32x16_f16 v[98:113], v[212:215], v[142:145], v[98:113]

.LBB0_851:
	s_cmp_ge_u32 s72, s90
	s_cbranch_scc1 .LBB0_865
	s_cmp_lt_u32 s74, s90
	v_cmp_eq_f32_e64 s[30:31], s1, v173
	s_cselect_b64 s[52:53], -1, 0
	s_cmp_ge_u32 s74, s90
	v_cndmask_b32_e64 v185, v173, 0, s[30:31]
	s_cbranch_scc1 .LBB0_854
	s_mul_i32 s34, s75, 0x6000
	v_add_u32_e32 v147, s34, v169
	ds_read_b128 v[148:151], v147
	v_xor_b32_e32 v2, 0x80000000, v185
	v_mov_b32_e32 v3, v2
	v_mov_b32_e32 v4, v2
	v_mov_b32_e32 v5, v2
	v_mov_b32_e32 v6, v2
	v_mov_b32_e32 v7, v2
	v_mov_b32_e32 v8, v2
	v_mov_b32_e32 v9, v2
	v_mov_b32_e32 v10, v2
	v_mov_b32_e32 v11, v2
	v_mov_b32_e32 v12, v2
	v_mov_b32_e32 v13, v2
	v_mov_b32_e32 v14, v2
	v_mov_b32_e32 v15, v2
	v_mov_b32_e32 v16, v2
	v_mov_b32_e32 v17, v2
	ds_read_b128 v[152:155], v147 offset:4096
	v_add_u32_e32 v147, s34, v170
	ds_read_b128 v[156:159], v147
	ds_read_b128 v[188:191], v147 offset:4096
	v_add_u32_e32 v147, s34, v171
	ds_read_b128 v[192:195], v147
	ds_read_b128 v[196:199], v147 offset:4096
	v_add_u32_e32 v147, s34, v172
	ds_read_b128 v[208:211], v147
	ds_read_b128 v[212:215], v147 offset:4096
	s_waitcnt lgkmcnt(7)
	s_nop 0
	v_mfma_f32_32x32x16_f16 v[18:33], v[148:151], v[130:133], v[2:17]
	s_waitcnt lgkmcnt(6)
	v_mfma_f32_32x32x16_f16 v[2:17], v[152:155], v[130:133], v[2:17]
	s_waitcnt lgkmcnt(5)
	v_mfma_f32_32x32x16_f16 v[18:33], v[156:159], v[134:137], v[18:33]
	s_waitcnt lgkmcnt(4)
	v_mfma_f32_32x32x16_f16 v[2:17], v[188:191], v[134:137], v[2:17]
	s_waitcnt lgkmcnt(3)
	v_mfma_f32_32x32x16_f16 v[18:33], v[192:195], v[138:141], v[18:33]
	s_waitcnt lgkmcnt(2)
	v_mfma_f32_32x32x16_f16 v[2:17], v[196:199], v[138:141], v[2:17]
	s_waitcnt lgkmcnt(1)
	v_mfma_f32_32x32x16_f16 v[18:33], v[208:211], v[142:145], v[18:33]
	s_waitcnt lgkmcnt(0)
	v_mfma_f32_32x32x16_f16 v[2:17], v[212:215], v[142:145], v[2:17]

.LBB0_878:
	s_add_i32 s30, s42, -1
	s_cmp_ge_u32 s30, s90
	s_cbranch_scc1 .LBB0_891
	s_cmp_lt_u32 s42, s90
	v_cmp_eq_f32_e64 s[30:31], s1, v172
	s_cselect_b64 s[40:41], -1, 0
	s_cmp_ge_u32 s42, s90
	v_cndmask_b32_e64 v184, v172, 0, s[30:31]
	s_cbranch_scc1 .LBB0_881
	s_mul_i32 s35, s26, 0x6000
	v_add_u32_e32 v147, s35, v168
	ds_read_b128 v[148:151], v147
	v_xor_b32_e32 v98, 0x80000000, v184
	v_mov_b32_e32 v99, v98
	v_mov_b32_e32 v100, v98
	v_mov_b32_e32 v101, v98
	v_mov_b32_e32 v102, v98
	v_mov_b32_e32 v103, v98
	v_mov_b32_e32 v104, v98
	v_mov_b32_e32 v105, v98
	v_mov_b32_e32 v106, v98
	v_mov_b32_e32 v107, v98
	v_mov_b32_e32 v108, v98
	v_mov_b32_e32 v109, v98
	v_mov_b32_e32 v110, v98
	v_mov_b32_e32 v111, v98
	v_mov_b32_e32 v112, v98
	v_mov_b32_e32 v113, v98
	ds_read_b128 v[152:155], v147 offset:4096
	v_add_u32_e32 v147, s35, v169
	ds_read_b128 v[156:159], v147
	ds_read_b128 v[188:191], v147 offset:4096
	v_add_u32_e32 v147, s35, v170
	ds_read_b128 v[192:195], v147
	ds_read_b128 v[196:199], v147 offset:4096
	v_add_u32_e32 v147, s35, v171
	ds_read_b128 v[208:211], v147
	ds_read_b128 v[212:215], v147 offset:4096
	s_waitcnt lgkmcnt(7)
	s_nop 0
	v_mfma_f32_32x32x16_f16 v[114:129], v[148:151], v[130:133], v[98:113]
	s_waitcnt lgkmcnt(6)
	v_mfma_f32_32x32x16_f16 v[98:113], v[152:155], v[130:133], v[98:113]
	s_waitcnt lgkmcnt(5)
	v_mfma_f32_32x32x16_f16 v[114:129], v[156:159], v[134:137], v[114:129]
	s_waitcnt lgkmcnt(4)
	v_mfma_f32_32x32x16_f16 v[98:113], v[188:191], v[134:137], v[98:113]
	s_waitcnt lgkmcnt(3)
	v_mfma_f32_32x32x16_f16 v[114:129], v[192:195], v[138:141], v[114:129]
	s_waitcnt lgkmcnt(2)
	v_mfma_f32_32x32x16_f16 v[98:113], v[196:199], v[138:141], v[98:113]
	s_waitcnt lgkmcnt(1)
	v_mfma_f32_32x32x16_f16 v[114:129], v[208:211], v[142:145], v[114:129]
	s_waitcnt lgkmcnt(0)
	v_mfma_f32_32x32x16_f16 v[98:113], v[212:215], v[142:145], v[98:113]

.LBB0_896:
	s_cmp_ge_u32 s42, s90
	s_cbranch_scc1 .LBB0_910
	s_cmp_lt_u32 s44, s90
	v_cmp_eq_f32_e64 s[30:31], s1, v172
	s_cselect_b64 s[40:41], -1, 0
	s_cmp_ge_u32 s44, s90
	v_cndmask_b32_e64 v184, v172, 0, s[30:31]
	s_cbranch_scc1 .LBB0_899
	s_mul_i32 s34, s45, 0x6000
	v_add_u32_e32 v147, s34, v168
	ds_read_b128 v[148:151], v147
	v_xor_b32_e32 v50, 0x80000000, v184
	v_mov_b32_e32 v51, v50
	v_mov_b32_e32 v52, v50
	v_mov_b32_e32 v53, v50
	v_mov_b32_e32 v54, v50
	v_mov_b32_e32 v55, v50
	v_mov_b32_e32 v56, v50
	v_mov_b32_e32 v57, v50
	v_mov_b32_e32 v58, v50
	v_mov_b32_e32 v59, v50
	v_mov_b32_e32 v60, v50
	v_mov_b32_e32 v61, v50
	v_mov_b32_e32 v62, v50
	v_mov_b32_e32 v63, v50
	v_mov_b32_e32 v64, v50
	v_mov_b32_e32 v65, v50
	ds_read_b128 v[152:155], v147 offset:4096
	v_add_u32_e32 v147, s34, v169
	ds_read_b128 v[156:159], v147
	ds_read_b128 v[188:191], v147 offset:4096
	v_add_u32_e32 v147, s34, v170
	ds_read_b128 v[192:195], v147
	ds_read_b128 v[196:199], v147 offset:4096
	v_add_u32_e32 v147, s34, v171
	ds_read_b128 v[208:211], v147
	ds_read_b128 v[212:215], v147 offset:4096
	s_waitcnt lgkmcnt(7)
	s_nop 0
	v_mfma_f32_32x32x16_f16 v[82:97], v[148:151], v[130:133], v[50:65]
	s_waitcnt lgkmcnt(6)
	v_mfma_f32_32x32x16_f16 v[50:65], v[152:155], v[130:133], v[50:65]
	s_waitcnt lgkmcnt(5)
	v_mfma_f32_32x32x16_f16 v[82:97], v[156:159], v[134:137], v[82:97]
	s_waitcnt lgkmcnt(4)
	v_mfma_f32_32x32x16_f16 v[50:65], v[188:191], v[134:137], v[50:65]
	s_waitcnt lgkmcnt(3)
	v_mfma_f32_32x32x16_f16 v[82:97], v[192:195], v[138:141], v[82:97]
	s_waitcnt lgkmcnt(2)
	v_mfma_f32_32x32x16_f16 v[50:65], v[196:199], v[138:141], v[50:65]
	s_waitcnt lgkmcnt(1)
	v_mfma_f32_32x32x16_f16 v[82:97], v[208:211], v[142:145], v[82:97]
	s_waitcnt lgkmcnt(0)
	v_mfma_f32_32x32x16_f16 v[50:65], v[212:215], v[142:145], v[50:65]
